# baseline (speedup 1.0000x reference)
_Z11gram_kernelPKfPKiS0_S0_S0_S0_S0_S0_S0_S0_S0_Pf:
	s_load_dwordx4 s[24:27], s[0:1], 0x0
	s_load_dwordx2 s[28:29], s[0:1], 0x40
	s_load_dwordx4 s[20:23], s[0:1], 0x30
	s_load_dwordx2 s[10:11], s[0:1], 0x58
	s_load_dwordx2 s[44:45], s[0:1], 0x20
	s_load_dwordx2 s[68:69], s[0:1], 0x10
	s_load_dwordx2 s[60:61], s[0:1], 0x18
	s_load_dwordx2 s[62:63], s[0:1], 0x28
	s_load_dwordx2 s[64:65], s[0:1], 0x48
	s_ashr_i32 s30, s2, 1
	v_mov_b32_e32 v11, 0
	s_ashr_i32 s31, s30, 31
	s_lshl_b32 s46, s30, 11
	s_lshl_b32 s3, s2, 10
	s_ashr_i32 s47, s46, 31
	s_and_b32 s33, s3, 0x400
	v_lshlrev_b32_e32 v46, 2, v0
	v_mov_b32_e32 v47, 0
	v_lshlrev_b32_e32 v212, 1, v0
	v_mov_b32_e32 v213, v47
	v_lshrrev_b32_e32 v219, 6, v0
	v_bfe_u32 v214, v0, 5, 1
	v_and_b32_e32 v220, 31, v0
	s_or_b32 s3, s46, s33
	v_lshlrev_b32_e32 v216, 4, v219
	v_lshlrev_b32_e32 v221, 3, v214
	v_or3_b32 v1, s3, v216, v221
	v_lshlrev_b32_e32 v232, 4, v220
	v_and_b32_e32 v218, 63, v0
	s_mov_b32 s39, 0x20000
	s_brev_b32 s38, 16
	v_lshl_or_b32 v180, v1, 9, v232
	v_add_u32_e32 v1, 0x10000, v180
	s_lshl_b64 s[4:5], s[46:47], 2
	s_lshl_b32 s3, s33, 2
	s_waitcnt lgkmcnt(0)
	s_mov_b64 s[36:37], s[24:25]
	s_and_b32 s37, s37, 0xffff
	s_add_u32 s26, s26, s4
	s_addc_u32 s27, s27, s5
	s_add_u32 s26, s26, s3
	s_addc_u32 s27, s27, 0
	v_lshl_add_u64 v[32:33], v[212:213], 2, s[26:27]
	global_load_dwordx2 v[32:33], v[32:33], off
	buffer_load_dwordx4 v[34:37], v180, s[36:39], 0 offen nt
	buffer_load_dwordx4 v[38:41], v180, s[36:39], 0 offen offset:512 nt
	buffer_load_dwordx4 v[42:45], v180, s[36:39], 0 offen offset:1024 nt
	buffer_load_dwordx4 v[96:99], v180, s[36:39], 0 offen offset:1536 nt
	buffer_load_dwordx4 v[100:103], v180, s[36:39], 0 offen offset:2048 nt
	buffer_load_dwordx4 v[104:107], v180, s[36:39], 0 offen offset:2560 nt
	buffer_load_dwordx4 v[108:111], v180, s[36:39], 0 offen offset:3072 nt
	buffer_load_dwordx4 v[112:115], v180, s[36:39], 0 offen offset:3584 nt
	buffer_load_dwordx4 v[116:119], v1, s[36:39], 0 offen nt
	buffer_load_dwordx4 v[120:123], v1, s[36:39], 0 offen offset:512 nt
	buffer_load_dwordx4 v[124:127], v1, s[36:39], 0 offen offset:1024 nt
	buffer_load_dwordx4 v[128:131], v1, s[36:39], 0 offen offset:1536 nt
	buffer_load_dwordx4 v[132:135], v1, s[36:39], 0 offen offset:2048 nt
	buffer_load_dwordx4 v[136:139], v1, s[36:39], 0 offen offset:2560 nt
	buffer_load_dwordx4 v[140:143], v1, s[36:39], 0 offen offset:3072 nt
	buffer_load_dwordx4 v[144:147], v1, s[36:39], 0 offen offset:3584 nt
	s_lshl_b64 s[4:5], s[30:31], 14
	s_add_u32 s48, s20, s4
	s_addc_u32 s49, s21, s5
	s_movk_i32 s3, 0x160
	v_cmp_gt_u32_e32 vcc, s3, v0
	s_mov_b32 s3, 0x10000
	v_lshrrev_b32_e32 v227, 5, v0
	v_and_b32_e32 v228, 0x7c, v46
	v_add_u32_e32 v2, 0x200, v0
	v_lshrrev_b32_e32 v229, 5, v2
	v_mul_u32_u24_e32 v246, 0x110, v227
	v_lshl_add_u32 v246, v220, 3, v246
	v_add_u32_e32 v246, 0x10000, v246
	v_lshlrev_b32_e32 v247, 2, v46
	s_waitcnt vmcnt(16)
	v_cmp_ne_u32_e64 s[6:7], 0, v32
	v_cmp_ne_u32_e64 s[4:5], 0, v33
	v_cmp_eq_u32_e64 s[8:9], 0, v218
	s_nop 0
	s_and_saveexec_b64 s[12:13], s[8:9]
	s_cbranch_execz .LBB0_6
	s_bcnt1_i32_b64 s6, s[6:7]
	s_bcnt1_i32_b64 s4, s[4:5]
	v_mov_b32_e32 v1, 0x21100
	s_add_i32 s4, s4, s6
	v_lshl_add_u32 v1, v219, 2, v1
	v_mov_b32_e32 v2, s4
	ds_write_b32 v1, v2

.LBB0_11:
	s_add_i32 s3, s3, 2
	s_cmp_gt_u32 s3, 5
	s_cselect_b64 vcc, -1, 0
	v_add_u32_e32 v184, 0xffff0000, v183
	s_and_b64 s[12:13], vcc, exec
	v_cndmask_b32_e32 v200, v184, v1, vcc
	s_cselect_b32 s15, 0x20000, 0x20000
	s_cselect_b32 s14, 0x10000, s16
	s_cselect_b32 s13, s41, s37
	s_cselect_b32 s12, s22, s36
	s_waitcnt vmcnt(8)
	v_cvt_pk_f16_f32 v187, v172, v176
	v_cvt_pk_f16_f32 v186, v160, v168
	v_cvt_pk_f16_f32 v185, v164, v156
	v_cvt_pk_f16_f32 v184, v148, v152
	v_cvt_pk_f16_f32 v191, v173, v177
	v_cvt_pk_f16_f32 v190, v161, v169
	v_cvt_pk_f16_f32 v189, v165, v157
	v_cvt_pk_f16_f32 v188, v149, v153
	v_cvt_pk_f16_f32 v195, v174, v178
	v_cvt_pk_f16_f32 v194, v162, v170
	v_cvt_pk_f16_f32 v193, v166, v158
	v_cvt_pk_f16_f32 v192, v150, v154
	v_cvt_pk_f16_f32 v199, v175, v179
	v_cvt_pk_f16_f32 v198, v163, v171
	v_cvt_pk_f16_f32 v197, v167, v159
	v_cvt_pk_f16_f32 v196, v151, v155
	buffer_load_dwordx4 v[148:151], v200, s[12:15], 0 offen nt
	buffer_load_dwordx4 v[152:155], v200, s[12:15], 0 offen offset:512 nt
	buffer_load_dwordx4 v[164:167], v200, s[12:15], 0 offen offset:1024 nt
	buffer_load_dwordx4 v[156:159], v200, s[12:15], 0 offen offset:1536 nt
	buffer_load_dwordx4 v[160:163], v200, s[12:15], 0 offen offset:2048 nt
	buffer_load_dwordx4 v[168:171], v200, s[12:15], 0 offen offset:2560 nt
	buffer_load_dwordx4 v[172:175], v200, s[12:15], 0 offen offset:3072 nt
	buffer_load_dwordx4 v[176:179], v200, s[12:15], 0 offen offset:3584 nt
	ds_write_b128 v180, v[184:187]
	ds_write_b128 v180, v[188:191] offset:1024
	ds_write_b128 v180, v[192:195] offset:2048
	ds_write_b128 v180, v[196:199] offset:3072
	s_cselect_b32 s14, s17, 0x8000000
	s_cselect_b32 s13, s29, s37
	s_cselect_b32 s12, s28, s36
	v_cndmask_b32_e32 v200, v183, v1, vcc
	s_cmp_lg_u32 s3, 0
	s_cbranch_scc1 .Lw47_not0
	global_load_dwordx4 v[48:51], v247, s[68:69]
	global_load_dwordx4 v[80:83], v247, s[44:45]
	v_add_u32_e32 v247, 0x2000, v247
	global_load_dwordx4 v[52:55], v247, s[68:69]
	global_load_dwordx4 v[84:87], v247, s[44:45]
	v_add_u32_e32 v247, 0x2000, v247
	global_load_dwordx4 v[56:59], v247, s[68:69]
	global_load_dwordx4 v[88:91], v247, s[44:45]
	v_add_u32_e32 v247, 0x2000, v247
	global_load_dwordx4 v[60:63], v247, s[68:69]
	global_load_dwordx4 v[92:95], v247, s[44:45]
	v_add_u32_e32 v247, 0x2000, v247
	global_load_dwordx4 v[64:67], v247, s[68:69]
	global_load_dwordx4 v[96:99], v247, s[44:45]
	v_add_u32_e32 v247, 0x2000, v247
	global_load_dwordx4 v[68:71], v247, s[68:69]
	global_load_dwordx4 v[100:103], v247, s[44:45]
	v_add_u32_e32 v247, 0x2000, v247
	global_load_dwordx4 v[72:75], v247, s[68:69]
	global_load_dwordx4 v[104:107], v247, s[44:45]
	v_add_u32_e32 v247, 0x2000, v247
	global_load_dwordx4 v[76:79], v247, s[68:69]
	global_load_dwordx4 v[108:111], v247, s[44:45]
	v_lshlrev_b32_e32 v251, 7, v0
	global_load_dword v250, v251, s[22:23]
	global_load_dword v250, v251, s[28:29]
	v_and_b32_e32 v251, 0x3fff, v251
	global_load_dword v250, v251, s[48:49]
	v_and_b32_e32 v251, 0x1fc, v46
	global_load_dword v250, v251, s[60:61]
	global_load_dword v250, v251, s[62:63]
	global_load_dword v250, v251, s[64:65]
	s_branch .Lw47_xdone

.Lw47_ydone:
	ds_read_b128 v[184:187], v181
	ds_read_b128 v[188:191], v182
	ds_read_b128 v[192:195], v182 offset:1024
	ds_read_b128 v[196:199], v181 offset:4096
	s_waitcnt lgkmcnt(2)
	v_mfma_f32_32x32x16_f16 v[18:33], v[184:187], v[188:191], v[18:33]
	s_waitcnt lgkmcnt(1)
	v_mfma_f32_32x32x16_f16 v[2:17], v[184:187], v[192:195], v[2:17]
	ds_read_b128 v[184:187], v182 offset:4096
	ds_read_b128 v[188:191], v182 offset:5120
	s_waitcnt lgkmcnt(1)
	v_mfma_f32_32x32x16_f16 v[18:33], v[196:199], v[184:187], v[18:33]
	s_waitcnt lgkmcnt(0)
	v_mfma_f32_32x32x16_f16 v[2:17], v[196:199], v[188:191], v[2:17]
	ds_read_b128 v[184:187], v181 offset:8192
	ds_read_b128 v[188:191], v182 offset:8192
	ds_read_b128 v[192:195], v182 offset:9216
	ds_read_b128 v[196:199], v181 offset:12288
	s_waitcnt lgkmcnt(2)
	v_mfma_f32_32x32x16_f16 v[18:33], v[184:187], v[188:191], v[18:33]
	s_waitcnt lgkmcnt(1)
	v_mfma_f32_32x32x16_f16 v[2:17], v[184:187], v[192:195], v[2:17]
	ds_read_b128 v[184:187], v182 offset:12288
	ds_read_b128 v[188:191], v182 offset:13312
	s_waitcnt lgkmcnt(1)
	v_mfma_f32_32x32x16_f16 v[18:33], v[196:199], v[184:187], v[18:33]
	s_waitcnt lgkmcnt(0)
	v_mfma_f32_32x32x16_f16 v[2:17], v[196:199], v[188:191], v[2:17]
	ds_read_b128 v[184:187], v181 offset:16384
	ds_read_b128 v[188:191], v182 offset:16384
	ds_read_b128 v[192:195], v182 offset:17408
	ds_read_b128 v[196:199], v181 offset:20480
	s_waitcnt lgkmcnt(2)
	v_mfma_f32_32x32x16_f16 v[18:33], v[184:187], v[188:191], v[18:33]
	s_waitcnt lgkmcnt(1)
	v_mfma_f32_32x32x16_f16 v[2:17], v[184:187], v[192:195], v[2:17]
	ds_read_b128 v[184:187], v182 offset:20480
	ds_read_b128 v[188:191], v182 offset:21504
	s_waitcnt lgkmcnt(1)
	v_mfma_f32_32x32x16_f16 v[18:33], v[196:199], v[184:187], v[18:33]
	s_waitcnt lgkmcnt(0)
	v_mfma_f32_32x32x16_f16 v[2:17], v[196:199], v[188:191], v[2:17]
	ds_read_b128 v[184:187], v181 offset:24576
	ds_read_b128 v[188:191], v182 offset:24576
	ds_read_b128 v[192:195], v182 offset:25600
	ds_read_b128 v[196:199], v181 offset:28672
	s_waitcnt lgkmcnt(2)
	v_mfma_f32_32x32x16_f16 v[18:33], v[184:187], v[188:191], v[18:33]
	s_waitcnt lgkmcnt(1)
	v_mfma_f32_32x32x16_f16 v[2:17], v[184:187], v[192:195], v[2:17]
	ds_read_b128 v[184:187], v182 offset:28672
	ds_read_b128 v[188:191], v182 offset:29696
	s_waitcnt lgkmcnt(1)
	v_mfma_f32_32x32x16_f16 v[18:33], v[196:199], v[184:187], v[18:33]
	s_waitcnt lgkmcnt(0)
	v_mfma_f32_32x32x16_f16 v[2:17], v[196:199], v[188:191], v[2:17]
	s_cmp_lg_u32 s3, 0
	s_cbranch_scc1 .Lw47_w8
	s_waitcnt vmcnt(30)
	s_branch .Lw47_wdone

.LBB0_13:
	s_or_saveexec_b64 s[10:11], s[10:11]
	v_mov_b32_e32 v217, 0
	s_xor_b64 exec, exec, s[10:11]
	s_cbranch_execz .LBB0_19
	s_nop 6
	v_add_u32_e32 v2, 0x20000, v180
	buffer_load_dwordx4 v[148:151], v2, s[36:39], 0 offen nt
	buffer_load_dwordx4 v[152:155], v2, s[36:39], 0 offen offset:512 nt
	buffer_load_dwordx4 v[164:167], v2, s[36:39], 0 offen offset:1024 nt
	buffer_load_dwordx4 v[156:159], v2, s[36:39], 0 offen offset:1536 nt
	buffer_load_dwordx4 v[160:163], v2, s[36:39], 0 offen offset:2048 nt
	buffer_load_dwordx4 v[168:171], v2, s[36:39], 0 offen offset:2560 nt
	buffer_load_dwordx4 v[172:175], v2, s[36:39], 0 offen offset:3072 nt
	buffer_load_dwordx4 v[176:179], v2, s[36:39], 0 offen offset:3584 nt
	v_lshlrev_b32_e32 v233, 4, v218
	s_waitcnt vmcnt(16)
	v_cvt_pk_f16_f32 v5, v108, v112
	v_cvt_pk_f16_f32 v4, v100, v104
	v_cvt_pk_f16_f32 v3, v42, v96
	v_cvt_pk_f16_f32 v2, v34, v38
	v_lshl_or_b32 v234, v219, 12, v233
	ds_write_b128 v234, v[2:5]
	v_cvt_pk_f16_f32 v5, v109, v113
	v_cvt_pk_f16_f32 v4, v101, v105
	v_cvt_pk_f16_f32 v3, v43, v97
	v_cvt_pk_f16_f32 v2, v35, v39
	ds_write_b128 v234, v[2:5] offset:1024
	v_cvt_pk_f16_f32 v5, v110, v114
	v_cvt_pk_f16_f32 v4, v102, v106
	v_cvt_pk_f16_f32 v3, v44, v98
	v_cvt_pk_f16_f32 v2, v36, v40
	s_movk_i32 s12, 0xf400
	ds_write_b128 v234, v[2:5] offset:2048
	v_cvt_pk_f16_f32 v5, v111, v115
	v_cvt_pk_f16_f32 v4, v103, v107
	v_cvt_pk_f16_f32 v3, v45, v99
	v_cvt_pk_f16_f32 v2, v37, v41
	v_mad_i32_i24 v235, v219, s12, v234
	s_add_i32 s12, s46, s33
	ds_write_b128 v234, v[2:5] offset:3072
	global_load_dwordx4 v[48:51], v247, s[68:69]
	global_load_dwordx4 v[80:83], v247, s[44:45]
	v_add_u32_e32 v247, 0x2000, v247
	global_load_dwordx4 v[52:55], v247, s[68:69]
	global_load_dwordx4 v[84:87], v247, s[44:45]
	v_add_u32_e32 v247, 0x2000, v247
	global_load_dwordx4 v[56:59], v247, s[68:69]
	global_load_dwordx4 v[88:91], v247, s[44:45]
	v_add_u32_e32 v247, 0x2000, v247
	global_load_dwordx4 v[60:63], v247, s[68:69]
	global_load_dwordx4 v[92:95], v247, s[44:45]
	v_add_u32_e32 v247, 0x2000, v247
	global_load_dwordx4 v[64:67], v247, s[68:69]
	global_load_dwordx4 v[96:99], v247, s[44:45]
	v_add_u32_e32 v247, 0x2000, v247
	global_load_dwordx4 v[68:71], v247, s[68:69]
	global_load_dwordx4 v[100:103], v247, s[44:45]
	v_add_u32_e32 v247, 0x2000, v247
	global_load_dwordx4 v[72:75], v247, s[68:69]
	global_load_dwordx4 v[104:107], v247, s[44:45]
	v_add_u32_e32 v247, 0x2000, v247
	global_load_dwordx4 v[76:79], v247, s[68:69]
	global_load_dwordx4 v[108:111], v247, s[44:45]
	v_lshlrev_b32_e32 v251, 7, v0
	global_load_dword v250, v251, s[22:23]
	global_load_dword v250, v251, s[28:29]
	v_and_b32_e32 v251, 0x3fff, v251
	global_load_dword v250, v251, s[48:49]
	v_and_b32_e32 v251, 0x1fc, v46
	global_load_dword v250, v251, s[60:61]
	global_load_dword v250, v251, s[62:63]
	global_load_dword v250, v251, s[64:65]
	v_add3_u32 v2, s12, v216, v221
	v_lshl_or_b32 v2, v2, 9, v232
	v_mov_b32_e32 v217, 0
	s_mov_b32 s3, 0
	v_add_u32_e32 v236, 0x40000, v2
	s_mov_b32 s16, 0x10000
	v_mov_b32_e32 v2, v217
	v_mov_b32_e32 v3, v217
	v_mov_b32_e32 v4, v217
	v_mov_b32_e32 v5, v217
	v_mov_b32_e32 v6, v217
	v_mov_b32_e32 v7, v217
	v_mov_b32_e32 v8, v217
	v_mov_b32_e32 v9, v217
	v_mov_b32_e32 v10, v217
	v_mov_b32_e32 v11, v217
	v_mov_b32_e32 v12, v217
	v_mov_b32_e32 v13, v217
	v_mov_b32_e32 v14, v217
	v_mov_b32_e32 v15, v217
	v_mov_b32_e32 v16, v217
	v_mov_b32_e32 v17, v217
	v_mov_b32_e32 v18, v217
	v_mov_b32_e32 v19, v217
	v_mov_b32_e32 v20, v217
	v_mov_b32_e32 v21, v217
	v_mov_b32_e32 v22, v217
	v_mov_b32_e32 v23, v217
	v_mov_b32_e32 v24, v217
	v_mov_b32_e32 v25, v217
	v_mov_b32_e32 v26, v217
	v_mov_b32_e32 v27, v217
	v_mov_b32_e32 v28, v217
	v_mov_b32_e32 v29, v217
	v_mov_b32_e32 v30, v217
	v_mov_b32_e32 v31, v217
	v_mov_b32_e32 v32, v217
	v_mov_b32_e32 v33, v217
	s_branch .LBB0_16

.Lw03_ydone:
	s_cmp_lg_u32 s3, 0
	s_cbranch_scc1 .Lw03_w8
	s_waitcnt vmcnt(30)
	s_branch .Lw03_wdone
